# P1 inner-loop header bookkeeping also hoisted into the loop-top MFMA run
# baseline (speedup 1.0000x reference)
.LBB2_32:
	s_xor_b64 s[30:31], s[4:5], -1
	s_lshl_b32 s4, s63, 8
	s_ashr_i32 s5, s4, 31
	s_lshl_b64 s[4:5], s[4:5], 11
	s_add_u32 s4, s14, s4
	s_addc_u32 s5, s15, s5
	s_add_u32 s24, s4, 0x400000
	s_addc_u32 s25, s5, 0
	s_and_b64 s[4:5], s[28:29], exec
	s_cselect_b32 s66, s25, s19
	s_cselect_b32 s67, s24, s18
	s_lshl_b32 s4, s62, 8
	s_ashr_i32 s5, s4, 31
	s_lshl_b64 s[4:5], s[4:5], 11
	s_add_u32 s26, s12, s4
	s_addc_u32 s27, s13, s5
	s_and_b64 s[4:5], s[28:29], exec
	s_cselect_b32 s68, s27, s1
	s_cselect_b32 s69, s26, s0
	s_add_u32 s70, s18, 0x40080
	s_addc_u32 s71, s19, 0
	s_add_u32 s72, s0, 0x100
	v_mov_b32_e32 v0, 0
	s_addc_u32 s73, s1, 0
	s_mov_b32 s74, -2
	v_mov_b32_e32 v1, v0
	v_mov_b32_e32 v2, v0
	v_mov_b32_e32 v3, v0
	v_mov_b32_e32 v4, v0
	v_mov_b32_e32 v5, v0
	v_mov_b32_e32 v6, v0
	v_mov_b32_e32 v7, v0
	v_mov_b32_e32 v8, v0
	v_mov_b32_e32 v9, v0
	v_mov_b32_e32 v10, v0
	v_mov_b32_e32 v11, v0
	v_mov_b32_e32 v16, v0
	v_mov_b32_e32 v17, v0
	v_mov_b32_e32 v18, v0
	v_mov_b32_e32 v19, v0
	v_mov_b32_e32 v24, v0
	v_mov_b32_e32 v25, v0
	v_mov_b32_e32 v26, v0
	v_mov_b32_e32 v27, v0
	v_mov_b32_e32 v32, v0
	v_mov_b32_e32 v33, v0
	v_mov_b32_e32 v34, v0
	v_mov_b32_e32 v35, v0
	v_mov_b32_e32 v40, v0
	v_mov_b32_e32 v41, v0
	v_mov_b32_e32 v42, v0
	v_mov_b32_e32 v43, v0
	v_mov_b32_e32 v48, v0
	v_mov_b32_e32 v49, v0
	v_mov_b32_e32 v50, v0
	v_mov_b32_e32 v51, v0
	v_mov_b32_e32 v12, v0
	v_mov_b32_e32 v13, v0
	v_mov_b32_e32 v14, v0
	v_mov_b32_e32 v15, v0
	v_mov_b32_e32 v20, v0
	v_mov_b32_e32 v21, v0
	v_mov_b32_e32 v22, v0
	v_mov_b32_e32 v23, v0
	v_mov_b32_e32 v28, v0
	v_mov_b32_e32 v29, v0
	v_mov_b32_e32 v30, v0
	v_mov_b32_e32 v31, v0
	v_mov_b32_e32 v36, v0
	v_mov_b32_e32 v37, v0
	v_mov_b32_e32 v38, v0
	v_mov_b32_e32 v39, v0
	v_mov_b32_e32 v44, v0
	v_mov_b32_e32 v45, v0
	v_mov_b32_e32 v46, v0
	v_mov_b32_e32 v47, v0
	v_mov_b32_e32 v52, v0
	v_mov_b32_e32 v53, v0
	v_mov_b32_e32 v54, v0
	v_mov_b32_e32 v55, v0
	v_mov_b32_e32 v56, v0
	v_mov_b32_e32 v57, v0
	v_mov_b32_e32 v58, v0
	v_mov_b32_e32 v59, v0
	v_mov_b32_e32 v60, v0
	v_mov_b32_e32 v61, v0
	v_mov_b32_e32 v62, v0
	v_mov_b32_e32 v63, v0
	v_mov_b32_e32 v64, v0
	v_mov_b32_e32 v65, v0
	v_mov_b32_e32 v66, v0
	v_mov_b32_e32 v67, v0
	v_mov_b32_e32 v68, v0
	v_mov_b32_e32 v69, v0
	v_mov_b32_e32 v70, v0
	v_mov_b32_e32 v71, v0
	v_mov_b32_e32 v76, v0
	v_mov_b32_e32 v77, v0
	v_mov_b32_e32 v78, v0
	v_mov_b32_e32 v79, v0
	v_mov_b32_e32 v84, v0
	v_mov_b32_e32 v85, v0
	v_mov_b32_e32 v86, v0
	v_mov_b32_e32 v87, v0
	v_mov_b32_e32 v92, v0
	v_mov_b32_e32 v93, v0
	v_mov_b32_e32 v94, v0
	v_mov_b32_e32 v95, v0
	v_mov_b32_e32 v100, v0
	v_mov_b32_e32 v101, v0
	v_mov_b32_e32 v102, v0
	v_mov_b32_e32 v103, v0
	v_mov_b32_e32 v112, v0
	v_mov_b32_e32 v113, v0
	v_mov_b32_e32 v114, v0
	v_mov_b32_e32 v115, v0
	v_mov_b32_e32 v116, v0
	v_mov_b32_e32 v117, v0
	v_mov_b32_e32 v118, v0
	v_mov_b32_e32 v119, v0
	v_mov_b32_e32 v72, v0
	v_mov_b32_e32 v73, v0
	v_mov_b32_e32 v74, v0
	v_mov_b32_e32 v75, v0
	v_mov_b32_e32 v80, v0
	v_mov_b32_e32 v81, v0
	v_mov_b32_e32 v82, v0
	v_mov_b32_e32 v83, v0
	v_mov_b32_e32 v88, v0
	v_mov_b32_e32 v89, v0
	v_mov_b32_e32 v90, v0
	v_mov_b32_e32 v91, v0
	v_mov_b32_e32 v96, v0
	v_mov_b32_e32 v97, v0
	v_mov_b32_e32 v98, v0
	v_mov_b32_e32 v99, v0
	v_mov_b32_e32 v104, v0
	v_mov_b32_e32 v105, v0
	v_mov_b32_e32 v106, v0
	v_mov_b32_e32 v107, v0
	v_mov_b32_e32 v108, v0
	v_mov_b32_e32 v109, v0
	v_mov_b32_e32 v110, v0
	v_mov_b32_e32 v111, v0
	v_mov_b32_e32 v120, v0
	v_mov_b32_e32 v121, v0
	v_mov_b32_e32 v122, v0
	v_mov_b32_e32 v123, v0
	s_waitcnt lgkmcnt(0)
	v_mov_b32_e32 v124, v0
	v_mov_b32_e32 v125, v0
	v_mov_b32_e32 v126, v0
	v_mov_b32_e32 v127, v0
	s_cmp_lg_u32 s74, 12
	s_cselect_b64 s[0:1], -1, 0
	s_and_b64 s[4:5], s[0:1], exec
	s_cselect_b32 s75, s73, s68
	s_cselect_b32 s16, s72, s69
	s_and_b32 s5, s71, 0xffff
	s_mov_b32 s4, s70
	s_or_b64 s[36:37], s[28:29], s[0:1]
	s_branch .LBB2_34
.LBB2_33:
	s_waitcnt vmcnt(6)
	s_barrier
	s_setprio 1
	v_mfma_i32_16x16x64_i8 v[48:51], v[144:147], v[184:187], v[48:51]
	s_add_i32 s74, s74, 2
	v_mfma_i32_16x16x64_i8 v[40:43], v[148:151], v[184:187], v[40:43]
	s_add_u32 s70, s70, 0x100
	s_addc_u32 s71, s71, 0
	v_mfma_i32_16x16x64_i8 v[32:35], v[144:147], v[172:175], v[32:35]
	s_add_u32 s72, s72, 0x100
	s_addc_u32 s73, s73, 0
	v_mfma_i32_16x16x64_i8 v[24:27], v[148:151], v[172:175], v[24:27]
	s_cmp_lg_u32 s74, 12
	s_cselect_b64 s[0:1], -1, 0
	v_mfma_i32_16x16x64_i8 v[16:19], v[144:147], v[168:171], v[16:19]
	s_and_b64 s[4:5], s[0:1], exec
	s_cselect_b32 s75, s73, s68
	s_cselect_b32 s16, s72, s69
	v_mfma_i32_16x16x64_i8 v[8:11], v[148:151], v[168:171], v[8:11]
	s_and_b32 s5, s71, 0xffff
	s_mov_b32 s4, s70
	v_mfma_i32_16x16x64_i8 v[4:7], v[144:147], v[160:163], v[4:7]
	s_or_b64 s[36:37], s[28:29], s[0:1]
	s_cmp_gt_u32 s74, 13
	v_mfma_i32_16x16x64_i8 v[0:3], v[148:151], v[160:163], v[0:3]
	v_mfma_i32_16x16x64_i8 v[48:51], v[156:159], v[188:191], v[48:51]
	v_mfma_i32_16x16x64_i8 v[40:43], v[152:155], v[188:191], v[40:43]
	v_mfma_i32_16x16x64_i8 v[32:35], v[156:159], v[176:179], v[32:35]
	v_mfma_i32_16x16x64_i8 v[24:27], v[152:155], v[176:179], v[24:27]
	v_mfma_i32_16x16x64_i8 v[16:19], v[156:159], v[180:183], v[16:19]
	v_mfma_i32_16x16x64_i8 v[8:11], v[152:155], v[180:183], v[8:11]
	v_mfma_i32_16x16x64_i8 v[4:7], v[156:159], v[164:167], v[4:7]
	v_mfma_i32_16x16x64_i8 v[0:3], v[152:155], v[164:167], v[0:3]
	s_setprio 0
	s_barrier
	s_cbranch_scc1 .LBB2_50
.LBB2_34:
	ds_read_b128 v[144:147], v203
	ds_read_b128 v[148:151], v203 offset:2048
	ds_read_b128 v[156:159], v204
	ds_read_b128 v[152:155], v204 offset:2048
	s_mov_b32 m0, s53
	ds_read_b128 v[184:187], v205
	ds_read_b128 v[172:175], v205 offset:2048
	ds_read_b128 v[188:191], v206
	ds_read_b128 v[176:179], v206 offset:2048
	ds_read_b128 v[168:171], v205 offset:4096
	ds_read_b128 v[160:163], v205 offset:6144
	ds_read_b128 v[180:183], v206 offset:4096
	ds_read_b128 v[164:167], v206 offset:6144
	buffer_load_dwordx4 v193, s[4:7], 0 offen lds
	s_mov_b32 m0, s54
	buffer_load_dwordx4 v197, s[4:7], 0 offen lds
	s_waitcnt lgkmcnt(8)
	s_barrier
	s_waitcnt lgkmcnt(0)
	s_setprio 1
	v_mfma_i32_16x16x64_i8 v[124:127], v[144:147], v[184:187], v[124:127]
	s_xor_b64 s[34:35], s[36:37], -1
	v_mfma_i32_16x16x64_i8 v[120:123], v[148:151], v[184:187], v[120:123]
	v_mfma_i32_16x16x64_i8 v[108:111], v[144:147], v[172:175], v[108:111]
	v_mfma_i32_16x16x64_i8 v[104:107], v[148:151], v[172:175], v[104:107]
	v_mfma_i32_16x16x64_i8 v[96:99], v[144:147], v[168:171], v[96:99]
	v_mfma_i32_16x16x64_i8 v[88:91], v[148:151], v[168:171], v[88:91]
	v_mfma_i32_16x16x64_i8 v[80:83], v[144:147], v[160:163], v[80:83]
	v_mfma_i32_16x16x64_i8 v[72:75], v[148:151], v[160:163], v[72:75]
	v_mfma_i32_16x16x64_i8 v[124:127], v[156:159], v[188:191], v[124:127]
	v_mfma_i32_16x16x64_i8 v[120:123], v[152:155], v[188:191], v[120:123]
	v_mfma_i32_16x16x64_i8 v[108:111], v[156:159], v[176:179], v[108:111]
	v_mfma_i32_16x16x64_i8 v[104:107], v[152:155], v[176:179], v[104:107]
	v_mfma_i32_16x16x64_i8 v[96:99], v[156:159], v[180:183], v[96:99]
	v_mfma_i32_16x16x64_i8 v[88:91], v[152:155], v[180:183], v[88:91]
	v_mfma_i32_16x16x64_i8 v[80:83], v[156:159], v[164:167], v[80:83]
	v_mfma_i32_16x16x64_i8 v[72:75], v[152:155], v[164:167], v[72:75]
	s_setprio 0
	s_barrier
	ds_read_b128 v[128:131], v207
	ds_read_b128 v[132:135], v207 offset:2048
	ds_read_b128 v[140:143], v208
	ds_read_b128 v[136:139], v208 offset:2048
	s_and_b64 vcc, exec, s[34:35]
	s_cbranch_vccnz .LBB2_36
	s_and_b32 s17, s75, 0xffff
	s_mov_b32 s18, s6
	s_mov_b32 s19, s7
	s_mov_b32 m0, s39
	s_nop 0
	buffer_load_dwordx4 v196, s[16:19], 0 offen lds
	s_mov_b32 m0, s40
	s_nop 0
	buffer_load_dwordx4 v198, s[16:19], 0 offen lds
